# gate/up GEMM epilogue: swiglu batches with packed f32 mul/add
# baseline (speedup 1.0000x reference)
.LBB0_1331:
	v_lshl_add_u32 v174, s30, 8, v153
	v_lshl_or_b32 v176, s29, 7, v141
	s_mov_b32 s100, 0xbfb8aa3b
	s_mov_b32 s101, 1.0
	v_ashrrev_i32_e32 v175, 31, v174
	v_ashrrev_i32_e32 v177, 31, v176
	v_lshlrev_b64 v[174:175], 12, v[174:175]
	v_lshlrev_b64 v[176:177], 1, v[176:177]
	v_lshl_add_u64 v[174:175], s[44:45], 0, v[174:175]
	v_lshl_add_u64 v[178:179], v[174:175], 0, v[176:177]
	v_pk_mul_f32 v[160:161], v[126:127], s[100:101] op_sel_hi:[1,0]
	v_pk_mul_f32 v[162:163], v[128:129], s[100:101] op_sel_hi:[1,0]
	v_pk_mul_f32 v[164:165], v[118:119], s[100:101] op_sel_hi:[1,0]
	v_pk_mul_f32 v[166:167], v[120:121], s[100:101] op_sel_hi:[1,0]
	v_exp_f32_e32 v160, v160
	v_exp_f32_e32 v161, v161
	v_exp_f32_e32 v162, v162
	v_exp_f32_e32 v163, v163
	v_exp_f32_e32 v164, v164
	v_exp_f32_e32 v165, v165
	v_exp_f32_e32 v166, v166
	v_exp_f32_e32 v167, v167
	v_pk_add_f32 v[160:161], v[160:161], s[100:101] op_sel:[0,1] op_sel_hi:[1,1]
	v_pk_add_f32 v[162:163], v[162:163], s[100:101] op_sel:[0,1] op_sel_hi:[1,1]
	v_pk_add_f32 v[164:165], v[164:165], s[100:101] op_sel:[0,1] op_sel_hi:[1,1]
	v_pk_add_f32 v[166:167], v[166:167], s[100:101] op_sel:[0,1] op_sel_hi:[1,1]
	v_rcp_f32_e32 v160, v160
	v_rcp_f32_e32 v161, v161
	v_rcp_f32_e32 v162, v162
	v_rcp_f32_e32 v163, v163
	v_rcp_f32_e32 v164, v164
	v_rcp_f32_e32 v165, v165
	v_rcp_f32_e32 v166, v166
	v_rcp_f32_e32 v167, v167
	v_pk_mul_f32 v[160:161], v[126:127], v[160:161]
	v_pk_mul_f32 v[162:163], v[128:129], v[162:163]
	v_pk_mul_f32 v[164:165], v[118:119], v[164:165]
	v_pk_mul_f32 v[166:167], v[120:121], v[166:167]
	v_pk_mul_f32 v[160:161], v[160:161], v[122:123]
	v_pk_mul_f32 v[162:163], v[162:163], v[124:125]
	v_pk_mul_f32 v[164:165], v[164:165], v[114:115]
	v_pk_mul_f32 v[166:167], v[166:167], v[116:117]
	v_cvt_pk_bf16_f32 v168, v160, v161
	v_cvt_pk_bf16_f32 v169, v162, v163
	v_cvt_pk_bf16_f32 v170, v164, v165
	v_cvt_pk_bf16_f32 v171, v166, v167
	global_store_dwordx4 v[178:179], v[168:171], off
	v_pk_mul_f32 v[160:161], v[110:111], s[100:101] op_sel_hi:[1,0]
	v_pk_mul_f32 v[162:163], v[112:113], s[100:101] op_sel_hi:[1,0]
	v_pk_mul_f32 v[164:165], v[102:103], s[100:101] op_sel_hi:[1,0]
	v_pk_mul_f32 v[166:167], v[104:105], s[100:101] op_sel_hi:[1,0]
	v_exp_f32_e32 v160, v160
	v_exp_f32_e32 v161, v161
	v_exp_f32_e32 v162, v162
	v_exp_f32_e32 v163, v163
	v_exp_f32_e32 v164, v164
	v_exp_f32_e32 v165, v165
	v_exp_f32_e32 v166, v166
	v_exp_f32_e32 v167, v167
	v_pk_add_f32 v[160:161], v[160:161], s[100:101] op_sel:[0,1] op_sel_hi:[1,1]
	v_pk_add_f32 v[162:163], v[162:163], s[100:101] op_sel:[0,1] op_sel_hi:[1,1]
	v_pk_add_f32 v[164:165], v[164:165], s[100:101] op_sel:[0,1] op_sel_hi:[1,1]
	v_pk_add_f32 v[166:167], v[166:167], s[100:101] op_sel:[0,1] op_sel_hi:[1,1]
	v_rcp_f32_e32 v160, v160
	v_rcp_f32_e32 v161, v161
	v_rcp_f32_e32 v162, v162
	v_rcp_f32_e32 v163, v163
	v_rcp_f32_e32 v164, v164
	v_rcp_f32_e32 v165, v165
	v_rcp_f32_e32 v166, v166
	v_rcp_f32_e32 v167, v167
	v_pk_mul_f32 v[160:161], v[110:111], v[160:161]
	v_pk_mul_f32 v[162:163], v[112:113], v[162:163]
	v_pk_mul_f32 v[164:165], v[102:103], v[164:165]
	v_pk_mul_f32 v[166:167], v[104:105], v[166:167]
	v_pk_mul_f32 v[160:161], v[160:161], v[106:107]
	v_pk_mul_f32 v[162:163], v[162:163], v[108:109]
	v_pk_mul_f32 v[164:165], v[164:165], v[98:99]
	v_pk_mul_f32 v[166:167], v[166:167], v[100:101]
	v_add_co_u32_e32 v172, vcc, 0x10000, v178
	v_cvt_pk_bf16_f32 v168, v160, v161
	v_cvt_pk_bf16_f32 v169, v162, v163
	v_cvt_pk_bf16_f32 v170, v164, v165
	v_cvt_pk_bf16_f32 v171, v166, v167
	v_addc_co_u32_e32 v173, vcc, 0, v179, vcc
	global_store_dwordx4 v[172:173], v[168:171], off
	v_pk_mul_f32 v[160:161], v[94:95], s[100:101] op_sel_hi:[1,0]
	v_pk_mul_f32 v[162:163], v[96:97], s[100:101] op_sel_hi:[1,0]
	v_pk_mul_f32 v[164:165], v[86:87], s[100:101] op_sel_hi:[1,0]
	v_pk_mul_f32 v[166:167], v[88:89], s[100:101] op_sel_hi:[1,0]
	v_exp_f32_e32 v160, v160
	v_exp_f32_e32 v161, v161
	v_exp_f32_e32 v162, v162
	v_exp_f32_e32 v163, v163
	v_exp_f32_e32 v164, v164
	v_exp_f32_e32 v165, v165
	v_exp_f32_e32 v166, v166
	v_exp_f32_e32 v167, v167
	v_pk_add_f32 v[160:161], v[160:161], s[100:101] op_sel:[0,1] op_sel_hi:[1,1]
	v_pk_add_f32 v[162:163], v[162:163], s[100:101] op_sel:[0,1] op_sel_hi:[1,1]
	v_pk_add_f32 v[164:165], v[164:165], s[100:101] op_sel:[0,1] op_sel_hi:[1,1]
	v_pk_add_f32 v[166:167], v[166:167], s[100:101] op_sel:[0,1] op_sel_hi:[1,1]
	v_rcp_f32_e32 v160, v160
	v_rcp_f32_e32 v161, v161
	v_rcp_f32_e32 v162, v162
	v_rcp_f32_e32 v163, v163
	v_rcp_f32_e32 v164, v164
	v_rcp_f32_e32 v165, v165
	v_rcp_f32_e32 v166, v166
	v_rcp_f32_e32 v167, v167
	v_pk_mul_f32 v[160:161], v[94:95], v[160:161]
	v_pk_mul_f32 v[162:163], v[96:97], v[162:163]
	v_pk_mul_f32 v[164:165], v[86:87], v[164:165]
	v_pk_mul_f32 v[166:167], v[88:89], v[166:167]
	v_pk_mul_f32 v[160:161], v[160:161], v[90:91]
	v_pk_mul_f32 v[162:163], v[162:163], v[92:93]
	v_pk_mul_f32 v[164:165], v[164:165], v[82:83]
	v_pk_mul_f32 v[166:167], v[166:167], v[84:85]
	v_add_co_u32_e32 v172, vcc, 0x20000, v178
	v_cvt_pk_bf16_f32 v168, v160, v161
	v_cvt_pk_bf16_f32 v169, v162, v163
	v_cvt_pk_bf16_f32 v170, v164, v165
	v_cvt_pk_bf16_f32 v171, v166, v167
	v_addc_co_u32_e32 v173, vcc, 0, v179, vcc
	global_store_dwordx4 v[172:173], v[168:171], off
	v_pk_mul_f32 v[160:161], v[78:79], s[100:101] op_sel_hi:[1,0]
	v_pk_mul_f32 v[162:163], v[80:81], s[100:101] op_sel_hi:[1,0]
	v_pk_mul_f32 v[164:165], v[70:71], s[100:101] op_sel_hi:[1,0]
	v_pk_mul_f32 v[166:167], v[72:73], s[100:101] op_sel_hi:[1,0]
	v_exp_f32_e32 v160, v160
	v_exp_f32_e32 v161, v161
	v_exp_f32_e32 v162, v162
	v_exp_f32_e32 v163, v163
	v_exp_f32_e32 v164, v164
	v_exp_f32_e32 v165, v165
	v_exp_f32_e32 v166, v166
	v_exp_f32_e32 v167, v167
	v_pk_add_f32 v[160:161], v[160:161], s[100:101] op_sel:[0,1] op_sel_hi:[1,1]
	v_pk_add_f32 v[162:163], v[162:163], s[100:101] op_sel:[0,1] op_sel_hi:[1,1]
	v_pk_add_f32 v[164:165], v[164:165], s[100:101] op_sel:[0,1] op_sel_hi:[1,1]
	v_pk_add_f32 v[166:167], v[166:167], s[100:101] op_sel:[0,1] op_sel_hi:[1,1]
	v_rcp_f32_e32 v160, v160
	v_rcp_f32_e32 v161, v161
	v_rcp_f32_e32 v162, v162
	v_rcp_f32_e32 v163, v163
	v_rcp_f32_e32 v164, v164
	v_rcp_f32_e32 v165, v165
	v_rcp_f32_e32 v166, v166
	v_rcp_f32_e32 v167, v167
	v_pk_mul_f32 v[160:161], v[78:79], v[160:161]
	v_pk_mul_f32 v[162:163], v[80:81], v[162:163]
	v_pk_mul_f32 v[164:165], v[70:71], v[164:165]
	v_pk_mul_f32 v[166:167], v[72:73], v[166:167]
	v_pk_mul_f32 v[160:161], v[160:161], v[74:75]
	v_pk_mul_f32 v[162:163], v[162:163], v[76:77]
	v_pk_mul_f32 v[164:165], v[164:165], v[66:67]
	v_pk_mul_f32 v[166:167], v[166:167], v[68:69]
	v_add_co_u32_e32 v172, vcc, 0x30000, v178
	v_cvt_pk_bf16_f32 v168, v160, v161
	v_cvt_pk_bf16_f32 v169, v162, v163
	v_cvt_pk_bf16_f32 v170, v164, v165
	v_cvt_pk_bf16_f32 v171, v166, v167
	v_addc_co_u32_e32 v173, vcc, 0, v179, vcc
	global_store_dwordx4 v[172:173], v[168:171], off
	v_pk_mul_f32 v[160:161], v[62:63], s[100:101] op_sel_hi:[1,0]
	v_pk_mul_f32 v[162:163], v[64:65], s[100:101] op_sel_hi:[1,0]
	v_pk_mul_f32 v[164:165], v[54:55], s[100:101] op_sel_hi:[1,0]
	v_pk_mul_f32 v[166:167], v[56:57], s[100:101] op_sel_hi:[1,0]
	v_exp_f32_e32 v160, v160
	v_exp_f32_e32 v161, v161
	v_exp_f32_e32 v162, v162
	v_exp_f32_e32 v163, v163
	v_exp_f32_e32 v164, v164
	v_exp_f32_e32 v165, v165
	v_exp_f32_e32 v166, v166
	v_exp_f32_e32 v167, v167
	v_pk_add_f32 v[160:161], v[160:161], s[100:101] op_sel:[0,1] op_sel_hi:[1,1]
	v_pk_add_f32 v[162:163], v[162:163], s[100:101] op_sel:[0,1] op_sel_hi:[1,1]
	v_pk_add_f32 v[164:165], v[164:165], s[100:101] op_sel:[0,1] op_sel_hi:[1,1]
	v_pk_add_f32 v[166:167], v[166:167], s[100:101] op_sel:[0,1] op_sel_hi:[1,1]
	v_rcp_f32_e32 v160, v160
	v_rcp_f32_e32 v161, v161
	v_rcp_f32_e32 v162, v162
	v_rcp_f32_e32 v163, v163
	v_rcp_f32_e32 v164, v164
	v_rcp_f32_e32 v165, v165
	v_rcp_f32_e32 v166, v166
	v_rcp_f32_e32 v167, v167
	v_pk_mul_f32 v[160:161], v[62:63], v[160:161]
	v_pk_mul_f32 v[162:163], v[64:65], v[162:163]
	v_pk_mul_f32 v[164:165], v[54:55], v[164:165]
	v_pk_mul_f32 v[166:167], v[56:57], v[166:167]
	v_pk_mul_f32 v[160:161], v[160:161], v[58:59]
	v_pk_mul_f32 v[162:163], v[162:163], v[60:61]
	v_pk_mul_f32 v[164:165], v[164:165], v[50:51]
	v_pk_mul_f32 v[166:167], v[166:167], v[52:53]
	v_add_co_u32_e32 v172, vcc, 0x80000, v178
	v_cvt_pk_bf16_f32 v168, v160, v161
	v_cvt_pk_bf16_f32 v169, v162, v163
	v_cvt_pk_bf16_f32 v170, v164, v165
	v_cvt_pk_bf16_f32 v171, v166, v167
	v_addc_co_u32_e32 v173, vcc, 0, v179, vcc
	global_store_dwordx4 v[172:173], v[168:171], off
	v_pk_mul_f32 v[160:161], v[46:47], s[100:101] op_sel_hi:[1,0]
	v_pk_mul_f32 v[162:163], v[48:49], s[100:101] op_sel_hi:[1,0]
	v_pk_mul_f32 v[164:165], v[38:39], s[100:101] op_sel_hi:[1,0]
	v_pk_mul_f32 v[166:167], v[40:41], s[100:101] op_sel_hi:[1,0]
	v_exp_f32_e32 v160, v160
	v_exp_f32_e32 v161, v161
	v_exp_f32_e32 v162, v162
	v_exp_f32_e32 v163, v163
	v_exp_f32_e32 v164, v164
	v_exp_f32_e32 v165, v165
	v_exp_f32_e32 v166, v166
	v_exp_f32_e32 v167, v167
	v_pk_add_f32 v[160:161], v[160:161], s[100:101] op_sel:[0,1] op_sel_hi:[1,1]
	v_pk_add_f32 v[162:163], v[162:163], s[100:101] op_sel:[0,1] op_sel_hi:[1,1]
	v_pk_add_f32 v[164:165], v[164:165], s[100:101] op_sel:[0,1] op_sel_hi:[1,1]
	v_pk_add_f32 v[166:167], v[166:167], s[100:101] op_sel:[0,1] op_sel_hi:[1,1]
	v_rcp_f32_e32 v160, v160
	v_rcp_f32_e32 v161, v161
	v_rcp_f32_e32 v162, v162
	v_rcp_f32_e32 v163, v163
	v_rcp_f32_e32 v164, v164
	v_rcp_f32_e32 v165, v165
	v_rcp_f32_e32 v166, v166
	v_rcp_f32_e32 v167, v167
	v_pk_mul_f32 v[160:161], v[46:47], v[160:161]
	v_pk_mul_f32 v[162:163], v[48:49], v[162:163]
	v_pk_mul_f32 v[164:165], v[38:39], v[164:165]
	v_pk_mul_f32 v[166:167], v[40:41], v[166:167]
	v_pk_mul_f32 v[160:161], v[160:161], v[42:43]
	v_pk_mul_f32 v[162:163], v[162:163], v[44:45]
	v_pk_mul_f32 v[164:165], v[164:165], v[34:35]
	v_pk_mul_f32 v[166:167], v[166:167], v[36:37]
	v_add_co_u32_e32 v172, vcc, 0x90000, v178
	v_cvt_pk_bf16_f32 v168, v160, v161
	v_cvt_pk_bf16_f32 v169, v162, v163
	v_cvt_pk_bf16_f32 v170, v164, v165
	v_cvt_pk_bf16_f32 v171, v166, v167
	v_addc_co_u32_e32 v173, vcc, 0, v179, vcc
	global_store_dwordx4 v[172:173], v[168:171], off
	v_pk_mul_f32 v[160:161], v[30:31], s[100:101] op_sel_hi:[1,0]
	v_pk_mul_f32 v[162:163], v[32:33], s[100:101] op_sel_hi:[1,0]
	v_pk_mul_f32 v[164:165], v[22:23], s[100:101] op_sel_hi:[1,0]
	v_pk_mul_f32 v[166:167], v[24:25], s[100:101] op_sel_hi:[1,0]
	v_exp_f32_e32 v160, v160
	v_exp_f32_e32 v161, v161
	v_exp_f32_e32 v162, v162
	v_exp_f32_e32 v163, v163
	v_exp_f32_e32 v164, v164
	v_exp_f32_e32 v165, v165
	v_exp_f32_e32 v166, v166
	v_exp_f32_e32 v167, v167
	v_pk_add_f32 v[160:161], v[160:161], s[100:101] op_sel:[0,1] op_sel_hi:[1,1]
	v_pk_add_f32 v[162:163], v[162:163], s[100:101] op_sel:[0,1] op_sel_hi:[1,1]
	v_pk_add_f32 v[164:165], v[164:165], s[100:101] op_sel:[0,1] op_sel_hi:[1,1]
	v_pk_add_f32 v[166:167], v[166:167], s[100:101] op_sel:[0,1] op_sel_hi:[1,1]
	v_rcp_f32_e32 v160, v160
	v_rcp_f32_e32 v161, v161
	v_rcp_f32_e32 v162, v162
	v_rcp_f32_e32 v163, v163
	v_rcp_f32_e32 v164, v164
	v_rcp_f32_e32 v165, v165
	v_rcp_f32_e32 v166, v166
	v_rcp_f32_e32 v167, v167
	v_pk_mul_f32 v[160:161], v[30:31], v[160:161]
	v_pk_mul_f32 v[162:163], v[32:33], v[162:163]
	v_pk_mul_f32 v[164:165], v[22:23], v[164:165]
	v_pk_mul_f32 v[166:167], v[24:25], v[166:167]
	v_pk_mul_f32 v[160:161], v[160:161], v[26:27]
	v_pk_mul_f32 v[162:163], v[162:163], v[28:29]
	v_pk_mul_f32 v[164:165], v[164:165], v[18:19]
	v_pk_mul_f32 v[166:167], v[166:167], v[20:21]
	v_add_co_u32_e32 v172, vcc, 0xa0000, v178
	v_cvt_pk_bf16_f32 v168, v160, v161
	v_cvt_pk_bf16_f32 v169, v162, v163
	v_cvt_pk_bf16_f32 v170, v164, v165
	v_cvt_pk_bf16_f32 v171, v166, v167
	v_addc_co_u32_e32 v173, vcc, 0, v179, vcc
	global_store_dwordx4 v[172:173], v[168:171], off
	v_pk_mul_f32 v[160:161], v[14:15], s[100:101] op_sel_hi:[1,0]
	v_pk_mul_f32 v[162:163], v[16:17], s[100:101] op_sel_hi:[1,0]
	v_pk_mul_f32 v[164:165], v[6:7], s[100:101] op_sel_hi:[1,0]
	v_pk_mul_f32 v[166:167], v[8:9], s[100:101] op_sel_hi:[1,0]
	v_exp_f32_e32 v160, v160
	v_exp_f32_e32 v161, v161
	v_exp_f32_e32 v162, v162
	v_exp_f32_e32 v163, v163
	v_exp_f32_e32 v164, v164
	v_exp_f32_e32 v165, v165
	v_exp_f32_e32 v166, v166
	v_exp_f32_e32 v167, v167
	v_pk_add_f32 v[160:161], v[160:161], s[100:101] op_sel:[0,1] op_sel_hi:[1,1]
	v_pk_add_f32 v[162:163], v[162:163], s[100:101] op_sel:[0,1] op_sel_hi:[1,1]
	v_pk_add_f32 v[164:165], v[164:165], s[100:101] op_sel:[0,1] op_sel_hi:[1,1]
	v_pk_add_f32 v[166:167], v[166:167], s[100:101] op_sel:[0,1] op_sel_hi:[1,1]
	v_rcp_f32_e32 v160, v160
	v_rcp_f32_e32 v161, v161
	v_rcp_f32_e32 v162, v162
	v_rcp_f32_e32 v163, v163
	v_rcp_f32_e32 v164, v164
	v_rcp_f32_e32 v165, v165
	v_rcp_f32_e32 v166, v166
	v_rcp_f32_e32 v167, v167
	v_pk_mul_f32 v[160:161], v[14:15], v[160:161]
	v_pk_mul_f32 v[162:163], v[16:17], v[162:163]
	v_pk_mul_f32 v[164:165], v[6:7], v[164:165]
	v_pk_mul_f32 v[166:167], v[8:9], v[166:167]
	v_pk_mul_f32 v[160:161], v[160:161], v[10:11]
	v_pk_mul_f32 v[162:163], v[162:163], v[12:13]
	v_pk_mul_f32 v[164:165], v[164:165], v[2:3]
	v_pk_mul_f32 v[166:167], v[166:167], v[4:5]
	v_add_co_u32_e32 v172, vcc, 0xb0000, v178
	v_cvt_pk_bf16_f32 v168, v160, v161
	v_cvt_pk_bf16_f32 v169, v162, v163
	v_cvt_pk_bf16_f32 v170, v164, v165
	v_cvt_pk_bf16_f32 v171, v166, v167
	v_addc_co_u32_e32 v173, vcc, 0, v179, vcc
	global_store_dwordx4 v[172:173], v[168:171], off
	s_mov_b64 s[0:1], -1
	s_and_b64 vcc, exec, s[2:3]
	s_cbranch_vccnz .LBB0_1322
	s_andn2_b64 vcc, exec, s[4:5]
	v_mov_b32 v2, 0
	s_cbranch_vccnz .LBB0_1321
	s_barrier
	s_branch .LBB0_1321
